# P12/P13 MoE unit dealing made XCD-aware: unit index = i*G + ((wg&7)*32 + (wg>>3)) so the 32 workgroups of one XCD take 32 consecutive units (shared A row tiles / W column tiles inside one L2)
# speedup vs baseline: 1.0069x; 1.0069x over previous
.LBB0_2312:
	s_or_b64 exec, exec, s[4:5]
	s_add_i32 s3, 0, 0x20200
	v_mov_b32_e32 v1, s3
	s_waitcnt lgkmcnt(0)
	s_barrier
	ds_read_b32 v1, v1
	s_lshr_b32 s32, s2, 3
	s_and_b32 s3, s2, 7
	s_lshl_b32 s3, s3, 5
	s_or_b32 s32, s32, s3
	s_cmpk_eq_u32 s48, 0x100
	s_cselect_b32 s32, s32, s2
	v_mul_lo_u32 v2, v3, s48
	v_add_u32_e32 v2, s32, v2
	s_waitcnt lgkmcnt(0)
	v_readfirstlane_b32 s3, v1
	s_lshl_b32 s3, s3, 4
	s_nop 0
	v_cmp_gt_i32_e64 s[4:5], s3, v2
	s_and_saveexec_b64 s[8:9], s[4:5]
	s_cbranch_execz .LBB0_2319
	s_mov_b64 s[10:11], 0
	s_brev_b32 s16, 1
	s_add_i32 s17, 0, 0x201fc
	s_add_i32 s18, 0, 0x20000
	v_mov_b32_e32 v4, 0x55098000
	s_mov_b32 s19, 0x3d40000

.LBB0_2317:
	v_mov_b32_e32 v5, s21
	ds_read_b32 v5, v5
	v_mov_b32_e32 v6, s20
	s_add_i32 s20, s20, 1
	s_add_i32 s21, s21, 4
	s_cmp_eq_u32 s20, 32
	s_waitcnt lgkmcnt(0)
	v_lshlrev_b32_e32 v5, 4, v5
	v_cmp_lt_i32_e64 s[4:5], v2, v5
	s_nop 1
	v_cndmask_b32_e64 v1, v6, v1, s[4:5]
	s_cbranch_scc0 .LBB0_2317
	v_lshl_add_u32 v5, v1, 2, s18
	ds_read2_b32 v[6:7], v5 offset0:32 offset1:64
	ds_read_b32 v5, v5 offset:384
	s_waitcnt lgkmcnt(1)
	v_sub_u32_e32 v8, 0, v7
	v_max_i32_e32 v8, v7, v8
	v_cvt_f32_u32_e32 v9, v8
	s_waitcnt lgkmcnt(0)
	v_lshlrev_b32_e32 v5, 4, v5
	v_sub_u32_e32 v11, 0, v8
	v_sub_u32_e32 v2, v2, v5
	v_rcp_iflag_f32_e32 v9, v9
	v_sub_u32_e32 v10, 0, v2
	v_max_i32_e32 v10, v2, v10
	v_xor_b32_e32 v5, v2, v7
	v_mul_f32_e32 v9, 0x4f7ffffe, v9
	v_cvt_u32_f32_e32 v9, v9
	v_ashrrev_i32_e32 v5, 31, v5
	v_mul_lo_u32 v11, v11, v9
	v_mul_hi_u32 v11, v9, v11
	v_add_u32_e32 v9, v9, v11
	v_mul_hi_u32 v9, v10, v9
	v_mul_lo_u32 v11, v9, v8
	v_sub_u32_e32 v10, v10, v11
	v_add_u32_e32 v12, 1, v9
	v_cmp_ge_u32_e64 s[4:5], v10, v8
	v_sub_u32_e32 v11, v10, v8
	s_nop 0
	v_cndmask_b32_e64 v9, v9, v12, s[4:5]
	v_cndmask_b32_e64 v10, v10, v11, s[4:5]
	v_add_u32_e32 v11, 1, v9
	v_cmp_ge_u32_e64 s[4:5], v10, v8
	v_lshl_add_u32 v10, v3, 4, s18
	v_add_u32_e32 v3, 0x200, v3
	v_cndmask_b32_e64 v8, v9, v11, s[4:5]
	v_xor_b32_e32 v8, v8, v5
	v_sub_u32_e32 v5, v8, v5
	v_mul_lo_u32 v7, v5, v7
	v_sub_u32_e32 v2, v2, v7
	v_lshl_add_u32 v2, v2, 8, v6
	v_lshlrev_b32_e32 v7, 19, v5
	v_lshlrev_b32_e32 v8, 23, v1
	v_lshl_or_b32 v9, v1, 8, v5
	v_mul_lo_u32 v1, v3, s48
	v_lshl_add_u32 v6, v2, 11, v4
	v_add3_u32 v7, v8, v7, s19
	v_ashrrev_i32_e32 v8, 8, v2
	v_add_u32_e32 v2, s32, v1
	v_cmp_le_i32_e64 s[4:5], s3, v2
	s_or_b64 s[10:11], s[4:5], s[10:11]
	ds_write_b128 v10, v[6:9] offset:1024
	s_andn2_b64 exec, exec, s[10:11]
	s_cbranch_execnz .LBB0_2314
.LBB0_2319:
	s_or_b64 exec, exec, s[8:9]
	s_and_saveexec_b64 s[4:5], vcc
	s_cbranch_execz .LBB0_2323
	s_cmp_le_i32 s3, s32
	s_mov_b32 s8, 0
	s_cbranch_scc1 .LBB0_2322
	s_abs_i32 s8, s48
	v_cvt_f32_u32_e32 v1, s8
	s_not_b32 s9, s32
	s_sub_i32 s10, 0, s8
	s_add_i32 s9, s48, s9
	v_rcp_iflag_f32_e32 v1, v1
	s_add_i32 s9, s9, s3
	s_xor_b32 s3, s9, s48
	s_abs_i32 s9, s9
	v_mul_f32_e32 v1, 0x4f7ffffe, v1
	v_cvt_u32_f32_e32 v1, v1
	s_ashr_i32 s3, s3, 31
	v_readfirstlane_b32 s11, v1
	s_mul_i32 s10, s10, s11
	s_mul_hi_u32 s10, s11, s10
	s_add_i32 s11, s11, s10
	s_mul_hi_u32 s10, s9, s11
	s_mul_i32 s11, s10, s8
	s_sub_i32 s9, s9, s11
	s_add_i32 s16, s10, 1
	s_sub_i32 s11, s9, s8
	s_cmp_ge_u32 s9, s8
	s_cselect_b32 s10, s16, s10
	s_cselect_b32 s9, s11, s9
	s_add_i32 s11, s10, 1
	s_cmp_ge_u32 s9, s8
	s_cselect_b32 s8, s11, s10
	s_xor_b32 s8, s8, s3
	s_sub_i32 s8, s8, s3

.LBB0_2400:
	s_add_i32 s3, 0, 0x20200
	v_mov_b32_e32 v1, s3
	ds_read_b32 v1, v1
	s_lshr_b32 s32, s2, 3
	s_and_b32 s3, s2, 7
	s_lshl_b32 s3, s3, 5
	s_or_b32 s32, s32, s3
	s_cmpk_eq_u32 s48, 0x100
	s_cselect_b32 s32, s32, s2
	v_mul_lo_u32 v2, v3, s48
	v_add_u32_e32 v2, s32, v2
	s_waitcnt lgkmcnt(0)
	v_readfirstlane_b32 s3, v1
	s_lshl_b32 s3, s3, 3
	s_nop 0
	v_cmp_gt_i32_e32 vcc, s3, v2
	s_and_saveexec_b64 s[6:7], vcc
	s_cbranch_execz .LBB0_2407
	s_mov_b64 s[8:9], 0
	s_brev_b32 s10, 1
	s_add_i32 s11, 0, 0x201fc
	s_add_i32 s12, 0, 0x20000
	v_mov_b32_e32 v4, 0x77098000
	s_mov_b32 s13, 0x23d40000
	v_mov_b32_e32 v5, v3

.LBB0_2405:
	v_mov_b32_e32 v6, s15
	ds_read_b32 v6, v6
	v_mov_b32_e32 v7, s14
	s_add_i32 s14, s14, 1
	s_add_i32 s15, s15, 4
	s_cmp_eq_u32 s14, 32
	s_waitcnt lgkmcnt(0)
	v_lshlrev_b32_e32 v6, 3, v6
	v_cmp_lt_i32_e32 vcc, v2, v6
	s_nop 1
	v_cndmask_b32_e32 v1, v7, v1, vcc
	s_cbranch_scc0 .LBB0_2405
	v_lshl_add_u32 v8, v1, 2, s12
	ds_read2_b32 v[6:7], v8 offset0:32 offset1:64
	ds_read_b32 v8, v8 offset:384
	s_waitcnt lgkmcnt(1)
	v_sub_u32_e32 v9, 0, v7
	v_max_i32_e32 v9, v7, v9
	v_cvt_f32_u32_e32 v10, v9
	s_waitcnt lgkmcnt(0)
	v_lshlrev_b32_e32 v8, 3, v8
	v_sub_u32_e32 v12, 0, v9
	v_sub_u32_e32 v2, v2, v8
	v_rcp_iflag_f32_e32 v10, v10
	v_sub_u32_e32 v11, 0, v2
	v_max_i32_e32 v11, v2, v11
	v_xor_b32_e32 v8, v2, v7
	v_mul_f32_e32 v10, 0x4f7ffffe, v10
	v_cvt_u32_f32_e32 v10, v10
	v_ashrrev_i32_e32 v8, 31, v8
	v_mul_lo_u32 v12, v12, v10
	v_mul_hi_u32 v12, v10, v12
	v_add_u32_e32 v10, v10, v12
	v_mul_hi_u32 v10, v11, v10
	v_mul_lo_u32 v12, v10, v9
	v_sub_u32_e32 v11, v11, v12
	v_add_u32_e32 v13, 1, v10
	v_cmp_ge_u32_e32 vcc, v11, v9
	v_sub_u32_e32 v12, v11, v9
	s_nop 0
	v_cndmask_b32_e32 v10, v10, v13, vcc
	v_cndmask_b32_e32 v11, v11, v12, vcc
	v_add_u32_e32 v12, 1, v10
	v_cmp_ge_u32_e32 vcc, v11, v9
	s_nop 1
	v_cndmask_b32_e32 v9, v10, v12, vcc
	v_xor_b32_e32 v9, v9, v8
	v_sub_u32_e32 v9, v9, v8
	v_mul_lo_u32 v7, v9, v7
	v_sub_u32_e32 v2, v2, v7
	v_lshl_add_u32 v10, v5, 4, s12
	v_add_u32_e32 v5, 0x200, v5
	v_lshl_add_u32 v2, v2, 8, v6
	v_lshlrev_b32_e32 v7, 19, v9
	v_lshlrev_b32_e32 v8, 22, v1
	v_lshl_or_b32 v9, v1, 8, v9
	v_mul_lo_u32 v1, v5, s48
	v_lshl_add_u32 v6, v2, 11, v4
	v_add3_u32 v7, v8, v7, s13
	v_ashrrev_i32_e32 v8, 8, v2
	v_add_u32_e32 v2, s32, v1
	v_cmp_le_i32_e32 vcc, s3, v2
	s_or_b64 s[8:9], vcc, s[8:9]
	ds_write_b128 v10, v[6:9] offset:1024
	s_andn2_b64 exec, exec, s[8:9]
	s_cbranch_execnz .LBB0_2402
.LBB0_2407:
	s_or_b64 exec, exec, s[6:7]
	s_mov_b32 s8, 0
	v_cmp_eq_u32_e32 vcc, 0, v3
	s_and_saveexec_b64 s[6:7], vcc
	s_cbranch_execz .LBB0_2411
	s_cmp_le_i32 s3, s32
	s_cbranch_scc1 .LBB0_2410
	s_abs_i32 s8, s48
	v_cvt_f32_u32_e32 v1, s8
	s_not_b32 s9, s32
	s_sub_i32 s10, 0, s8
	s_add_i32 s9, s48, s9
	v_rcp_iflag_f32_e32 v1, v1
	s_add_i32 s9, s9, s3
	s_xor_b32 s3, s9, s48
	s_abs_i32 s9, s9
	v_mul_f32_e32 v1, 0x4f7ffffe, v1
	v_cvt_u32_f32_e32 v1, v1
	s_ashr_i32 s3, s3, 31
	v_readfirstlane_b32 s11, v1
	s_mul_i32 s10, s10, s11
	s_mul_hi_u32 s10, s11, s10
	s_add_i32 s11, s11, s10
	s_mul_hi_u32 s10, s9, s11
	s_mul_i32 s11, s10, s8
	s_sub_i32 s9, s9, s11
	s_add_i32 s12, s10, 1
	s_sub_i32 s11, s9, s8
	s_cmp_ge_u32 s9, s8
	s_cselect_b32 s10, s12, s10
	s_cselect_b32 s9, s11, s9
	s_add_i32 s11, s10, 1
	s_cmp_ge_u32 s9, s8
	s_cselect_b32 s8, s11, s10
	s_xor_b32 s8, s8, s3
	s_sub_i32 s8, s8, s3
